# removed the dead staging of out-of-range sub-loads in the two peeled final steps (LDS waits recounted)
# speedup vs baseline: 1.0022x; 1.0022x over previous
.LBB1_16:
	s_load_dwordx4 s[4:7], s[0:1], 0x18
	v_or_b32_e32 v168, 0x10000, v204
	v_xor_b32_e32 v162, 0x80, v203
	v_add_u32_e32 v158, v168, v162
	ds_read_b128 v[146:149], v158
	ds_read_b128 v[150:153], v158 offset:16384
	ds_read_b128 v[154:157], v158 offset:32768
	ds_read_b128 v[158:161], v158 offset:49152
	v_or_b32_e32 v169, 0x24000, v204
	v_add_u32_e32 v162, v169, v162
	ds_read_b128 v[162:165], v162
	s_waitcnt vmcnt(11)
	s_waitcnt vmcnt(10)
	s_waitcnt lgkmcnt(0)
	v_mfma_f32_32x32x16_f16 v[50:65], v[118:121], v[154:157], v[50:65]
	v_xor_b32_e32 v156, 0xa0, v203
	v_add_u32_e32 v138, v169, v156
	v_mfma_f32_32x32x16_f16 v[2:17], v[118:121], v[146:149], v[2:17]
	v_mfma_f32_32x32x16_f16 v[34:49], v[118:121], v[150:153], v[34:49]
	v_add_u32_e32 v150, v168, v156
	v_mfma_f32_32x32x16_f16 v[18:33], v[118:121], v[158:161], v[18:33]
	ds_read_b128 v[118:121], v150
	ds_read_b128 v[142:145], v150 offset:16384
	ds_read_b128 v[146:149], v150 offset:32768
	ds_read_b128 v[150:153], v150 offset:49152
	ds_read_b128 v[138:141], v138
	v_mfma_f32_32x32x16_f16 v[66:81], v[114:117], v[162:165], v[66:81]
	s_waitcnt vmcnt(9)
	s_waitcnt vmcnt(8)
	s_waitcnt lgkmcnt(4)
	v_mfma_f32_32x32x16_f16 v[2:17], v[90:93], v[118:121], v[2:17]
	s_waitcnt lgkmcnt(3)
	v_mfma_f32_32x32x16_f16 v[34:49], v[90:93], v[142:145], v[34:49]
	s_waitcnt lgkmcnt(2)
	v_mfma_f32_32x32x16_f16 v[50:65], v[90:93], v[146:149], v[50:65]
	s_waitcnt lgkmcnt(1)
	v_mfma_f32_32x32x16_f16 v[18:33], v[90:93], v[150:153], v[18:33]
	s_waitcnt lgkmcnt(0)
	v_mfma_f32_32x32x16_f16 v[66:81], v[98:101], v[138:141], v[66:81]
	v_xor_b32_e32 v130, 0xc0, v203
	v_add_u32_e32 v118, v168, v130
	ds_read_b128 v[90:93], v118
	ds_read_b128 v[98:101], v118 offset:16384
	ds_read_b128 v[114:117], v118 offset:32768
	ds_read_b128 v[118:121], v118 offset:49152
	v_add_u32_e32 v130, v169, v130
	ds_read_b128 v[130:133], v130
	s_waitcnt vmcnt(3)
	s_waitcnt vmcnt(2)
	v_xor_b32_e32 v134, 0xe0, v203
	s_waitcnt lgkmcnt(4)
	v_mfma_f32_32x32x16_f16 v[2:17], v[102:105], v[90:93], v[2:17]
	s_waitcnt lgkmcnt(3)
	v_mfma_f32_32x32x16_f16 v[34:49], v[102:105], v[98:101], v[34:49]
	s_waitcnt lgkmcnt(2)
	v_mfma_f32_32x32x16_f16 v[50:65], v[102:105], v[114:117], v[50:65]
	v_add_u32_e32 v114, v168, v134
	s_waitcnt lgkmcnt(1)
	v_mfma_f32_32x32x16_f16 v[18:33], v[102:105], v[118:121], v[18:33]
	ds_read_b128 v[90:93], v114
	ds_read_b128 v[98:101], v114 offset:16384
	ds_read_b128 v[102:105], v114 offset:32768
	ds_read_b128 v[114:117], v114 offset:49152
	v_add_u32_e32 v118, v169, v134
	ds_read_b128 v[118:121], v118
	s_waitcnt lgkmcnt(5)
	v_mfma_f32_32x32x16_f16 v[66:81], v[94:97], v[130:133], v[66:81]
	s_waitcnt vmcnt(1)
	s_waitcnt vmcnt(0)
	s_waitcnt lgkmcnt(4)
	v_mfma_f32_32x32x16_f16 v[2:17], v[82:85], v[90:93], v[2:17]
	s_waitcnt lgkmcnt(3)
	v_mfma_f32_32x32x16_f16 v[34:49], v[82:85], v[98:101], v[34:49]
	s_waitcnt lgkmcnt(2)
	v_mfma_f32_32x32x16_f16 v[50:65], v[82:85], v[102:105], v[50:65]
	s_waitcnt lgkmcnt(1)
	v_mfma_f32_32x32x16_f16 v[18:33], v[82:85], v[114:117], v[18:33]
	s_waitcnt lgkmcnt(0)
	v_mfma_f32_32x32x16_f16 v[66:81], v[86:89], v[118:121], v[66:81]
	v_mbcnt_lo_u32_b32 v82, -1, 0
	v_mbcnt_hi_u32_b32 v82, -1, v82
	v_and_b32_e32 v83, 64, v82
	v_xor_b32_e32 v87, 16, v82
	v_add_u32_e32 v83, 64, v83
	v_and_b32_e32 v84, 16, v0
	v_cmp_lt_i32_e32 vcc, v87, v83
	v_and_b32_e32 v85, 8, v0
	v_and_b32_e32 v86, 4, v0
	v_cndmask_b32_e32 v87, v82, v87, vcc
	v_cmp_eq_u32_e32 vcc, 0, v84
	v_lshlrev_b32_e32 v228, 2, v87
	s_waitcnt lgkmcnt(0)
	v_cndmask_b32_e32 v84, v74, v66, vcc
	v_cndmask_b32_e32 v66, v66, v74, vcc
	v_cndmask_b32_e32 v74, v67, v75, vcc
	ds_bpermute_b32 v74, v228, v74
	v_cndmask_b32_e32 v67, v75, v67, vcc
	v_cndmask_b32_e32 v75, v70, v78, vcc
	ds_bpermute_b32 v75, v228, v75
	v_cndmask_b32_e32 v87, v68, v76, vcc
	s_waitcnt lgkmcnt(1)
	v_add_f32_e32 v67, v67, v74
	v_cndmask_b32_e32 v74, v77, v69, vcc
	v_cndmask_b32_e32 v69, v69, v77, vcc
	ds_bpermute_b32 v69, v228, v69
	v_cndmask_b32_e32 v68, v76, v68, vcc
	v_cndmask_b32_e32 v76, v71, v79, vcc
	ds_bpermute_b32 v76, v228, v76
	ds_bpermute_b32 v66, v228, v66
	v_cndmask_b32_e32 v70, v78, v70, vcc
	s_waitcnt lgkmcnt(2)
	v_add_f32_e32 v69, v74, v69
	v_add_f32_e32 v70, v70, v75
	v_cndmask_b32_e32 v74, v72, v80, vcc
	v_cndmask_b32_e32 v75, v73, v81, vcc
	ds_bpermute_b32 v87, v228, v87
	v_cndmask_b32_e32 v71, v79, v71, vcc
	ds_bpermute_b32 v74, v228, v74
	ds_bpermute_b32 v75, v228, v75
	s_waitcnt lgkmcnt(4)
	v_add_f32_e32 v71, v71, v76
	v_xor_b32_e32 v76, 8, v82
	v_cmp_lt_i32_e64 s[0:1], v76, v83
	s_waitcnt lgkmcnt(3)
	v_add_f32_e32 v66, v84, v66
	s_waitcnt lgkmcnt(2)
	v_add_f32_e32 v68, v68, v87
	v_cndmask_b32_e64 v76, v82, v76, s[0:1]
	v_cmp_eq_u32_e64 s[0:1], 0, v85
	v_lshlrev_b32_e32 v229, 2, v76
	s_barrier
	v_cndmask_b32_e64 v76, v70, v66, s[0:1]
	v_cndmask_b32_e64 v66, v66, v70, s[0:1]
	v_cndmask_b32_e32 v70, v80, v72, vcc
	v_cndmask_b32_e32 v72, v81, v73, vcc
	s_waitcnt lgkmcnt(1)
	v_add_f32_e32 v70, v70, v74
	s_waitcnt lgkmcnt(0)
	v_add_f32_e32 v72, v72, v75
	v_cndmask_b32_e64 v73, v71, v67, s[0:1]
	v_cndmask_b32_e64 v67, v67, v71, s[0:1]
	v_cndmask_b32_e64 v71, v68, v70, s[0:1]
	v_cndmask_b32_e64 v74, v69, v72, s[0:1]
	ds_bpermute_b32 v66, v229, v66
	ds_bpermute_b32 v67, v229, v67
	ds_bpermute_b32 v71, v229, v71
	ds_bpermute_b32 v74, v229, v74
	v_cndmask_b32_e64 v68, v70, v68, s[0:1]
	v_xor_b32_e32 v70, 4, v82
	v_cndmask_b32_e64 v69, v72, v69, s[0:1]
	v_cmp_lt_i32_e32 vcc, v70, v83
	s_waitcnt lgkmcnt(3)
	v_add_f32_e32 v66, v76, v66
	s_waitcnt lgkmcnt(2)
	v_add_f32_e32 v67, v73, v67
	s_waitcnt lgkmcnt(1)
	v_add_f32_e32 v68, v68, v71
	s_waitcnt lgkmcnt(0)
	v_add_f32_e32 v69, v69, v74
	v_cndmask_b32_e32 v70, v82, v70, vcc
	v_cmp_eq_u32_e32 vcc, 0, v86
	v_lshlrev_b32_e32 v230, 2, v70
	v_and_b32_e32 v71, 2, v0
	v_cndmask_b32_e32 v70, v68, v66, vcc
	v_cndmask_b32_e32 v66, v66, v68, vcc
	v_cndmask_b32_e32 v68, v67, v69, vcc
	ds_bpermute_b32 v66, v230, v66
	ds_bpermute_b32 v68, v230, v68
	v_cndmask_b32_e32 v67, v69, v67, vcc
	v_cmp_eq_u32_e32 vcc, 0, v71
	s_waitcnt lgkmcnt(0)
	v_add_f32_e32 v66, v70, v66
	v_add_f32_e32 v67, v67, v68
	v_cndmask_b32_e32 v68, v67, v66, vcc
	v_cndmask_b32_e32 v66, v66, v67, vcc
	v_xor_b32_e32 v67, 2, v82
	v_cmp_lt_i32_e32 vcc, v67, v83
	s_nop 1
	v_cndmask_b32_e32 v67, v82, v67, vcc
	v_lshlrev_b32_e32 v231, 2, v67
	ds_bpermute_b32 v66, v231, v66
	v_xor_b32_e32 v67, 1, v82
	v_cmp_lt_i32_e32 vcc, v67, v83
	s_waitcnt lgkmcnt(0)
	v_add_f32_e32 v66, v68, v66
	v_cndmask_b32_e32 v67, v82, v67, vcc
	v_lshlrev_b32_e32 v232, 2, v67
	ds_bpermute_b32 v67, v232, v66
	v_cmp_eq_u32_e32 vcc, 0, v196
	s_and_saveexec_b64 s[0:1], vcc
	s_cbranch_execz .LBB1_18
	s_lshl_b32 s20, s2, 8
	s_waitcnt lgkmcnt(0)
	v_add_f32_e32 v68, v66, v67
	v_lshl_or_b32 v66, v225, 7, s20
	v_lshlrev_b32_e32 v67, 5, v224
	v_bfe_u32 v69, v0, 1, 2
	v_or3_b32 v66, v66, v67, v69
	v_and_b32_e32 v67, 24, v0
	v_lshlrev_b32_e32 v69, 2, v1
	v_or3_b32 v66, v66, v67, v69
	v_ashrrev_i32_e32 v67, 31, v66
	v_lshl_add_u64 v[66:67], v[66:67], 2, s[4:5]
	global_store_dword v[66:67], v68, off sc1
